# attn_fast S^T: two batches of 16 LDS reads + 16 back-to-back MFMAs instead of read-pair/wait/MFMA (single wave per SIMD in that phase now)
# baseline (speedup 1.0000x reference)
.LBB12_15:
	v_add_u32_e32 v79, s33, v70
	v_bitop3_b32 v68, v70, s6, v1 bitop3:0x48
	v_readfirstlane_b32 s8, v79
	v_lshl_add_u64 v[80:81], v[66:67], 0, v[68:69]
	s_mov_b32 m0, s8
	v_add_u32_e32 v68, 0x200, v1
	global_load_lds_dwordx4 v[80:81], off
	v_cmp_lt_u32_e32 vcc, s7, v1
	v_add_u32_e32 v70, 0x2000, v70
	v_lshl_add_u64 v[66:67], v[66:67], 0, s[4:5]
	s_or_b64 s[0:1], vcc, s[0:1]
	v_mov_b32_e32 v1, v68
	s_andn2_b64 exec, exec, s[0:1]
	s_cbranch_execnz .LBB12_15
	s_or_b64 exec, exec, s[0:1]
	v_readfirstlane_b32 s44, v0
	s_nop 3
	s_cmp_lt_u32 s44, 0x100
	s_cbranch_scc0 .Lat_dh1
	v_lshl_add_u32 v1, v103, 9, 0
	v_add_u32_e32 v114, v1, v78
	v_add_u32_e32 v117, v1, v77
	v_add_u32_e32 v115, v1, v76
	v_add_u32_e32 v113, v1, v75
	v_add_u32_e32 v119, v1, v74
	v_add_u32_e32 v118, v1, v72
	v_add_u32_e32 v116, v1, v73
	v_add_u32_e32 v1, v1, v71
	s_mov_b32 s38, 0x5040100
	s_add_u32 s36, s30, s34
	s_addc_u32 s37, s31, s35
	s_add_i32 s30, 0, 0x20000
	v_lshlrev_b32_e32 v112, 7, v103
	s_add_i32 s34, 0, 0x22000
	ds_read_b128 v[156:159], v114
	ds_read_b128 v[160:163], v117
	ds_read_b128 v[164:167], v115
	ds_read_b128 v[168:171], v113
	ds_read_b128 v[172:175], v119
	ds_read_b128 v[176:179], v118
	ds_read_b128 v[180:183], v116
	ds_read_b128 v[184:187], v1
	ds_read_b128 v[188:191], v114 offset:8192
	ds_read_b128 v[192:195], v117 offset:8192
	ds_read_b128 v[196:199], v115 offset:8192
	ds_read_b128 v[200:203], v113 offset:8192
	ds_read_b128 v[204:207], v119 offset:8192
	ds_read_b128 v[208:211], v118 offset:8192
	ds_read_b128 v[212:215], v116 offset:8192
	ds_read_b128 v[216:219], v1 offset:8192
	s_waitcnt lgkmcnt(8)
	v_mfma_f32_16x16x32_bf16 v[66:69], v[156:159], v[62:65], 0
	v_mfma_f32_16x16x32_bf16 v[66:69], v[160:163], v[58:61], v[66:69]
	v_mfma_f32_16x16x32_bf16 v[66:69], v[164:167], v[54:57], v[66:69]
	v_mfma_f32_16x16x32_bf16 v[66:69], v[168:171], v[50:53], v[66:69]
	v_mfma_f32_16x16x32_bf16 v[66:69], v[172:175], v[46:49], v[66:69]
	v_mfma_f32_16x16x32_bf16 v[66:69], v[176:179], v[42:45], v[66:69]
	v_mfma_f32_16x16x32_bf16 v[66:69], v[180:183], v[38:41], v[66:69]
	v_mfma_f32_16x16x32_bf16 v[66:69], v[184:187], v[34:37], v[66:69]
	s_waitcnt lgkmcnt(0)
	v_mfma_f32_16x16x32_bf16 v[70:73], v[188:191], v[62:65], 0
	v_mfma_f32_16x16x32_bf16 v[70:73], v[192:195], v[58:61], v[70:73]
	v_mfma_f32_16x16x32_bf16 v[70:73], v[196:199], v[54:57], v[70:73]
	v_mfma_f32_16x16x32_bf16 v[70:73], v[200:203], v[50:53], v[70:73]
	v_mfma_f32_16x16x32_bf16 v[70:73], v[204:207], v[46:49], v[70:73]
	v_mfma_f32_16x16x32_bf16 v[70:73], v[208:211], v[42:45], v[70:73]
	v_mfma_f32_16x16x32_bf16 v[70:73], v[212:215], v[38:41], v[70:73]
	v_mfma_f32_16x16x32_bf16 v[70:73], v[216:219], v[34:37], v[70:73]
	ds_read_b128 v[156:159], v114 offset:16384
	ds_read_b128 v[160:163], v117 offset:16384
	ds_read_b128 v[164:167], v115 offset:16384
	ds_read_b128 v[168:171], v113 offset:16384
	ds_read_b128 v[172:175], v119 offset:16384
	ds_read_b128 v[176:179], v118 offset:16384
	ds_read_b128 v[180:183], v116 offset:16384
	ds_read_b128 v[184:187], v1 offset:16384
	ds_read_b128 v[188:191], v114 offset:24576
	ds_read_b128 v[192:195], v117 offset:24576
	ds_read_b128 v[196:199], v115 offset:24576
	ds_read_b128 v[200:203], v113 offset:24576
	ds_read_b128 v[204:207], v119 offset:24576
	ds_read_b128 v[208:211], v118 offset:24576
	ds_read_b128 v[212:215], v116 offset:24576
	ds_read_b128 v[216:219], v1 offset:24576
	s_waitcnt lgkmcnt(8)
	v_mfma_f32_16x16x32_bf16 v[74:77], v[156:159], v[62:65], 0
	v_mfma_f32_16x16x32_bf16 v[74:77], v[160:163], v[58:61], v[74:77]
	v_mfma_f32_16x16x32_bf16 v[74:77], v[164:167], v[54:57], v[74:77]
	v_mfma_f32_16x16x32_bf16 v[74:77], v[168:171], v[50:53], v[74:77]
	v_mfma_f32_16x16x32_bf16 v[74:77], v[172:175], v[46:49], v[74:77]
	v_mfma_f32_16x16x32_bf16 v[74:77], v[176:179], v[42:45], v[74:77]
	v_mfma_f32_16x16x32_bf16 v[74:77], v[180:183], v[38:41], v[74:77]
	v_mfma_f32_16x16x32_bf16 v[74:77], v[184:187], v[34:37], v[74:77]
	s_waitcnt lgkmcnt(0)
	v_mfma_f32_16x16x32_bf16 v[220:223], v[188:191], v[62:65], 0
	v_mfma_f32_16x16x32_bf16 v[220:223], v[192:195], v[58:61], v[220:223]
	v_mfma_f32_16x16x32_bf16 v[220:223], v[196:199], v[54:57], v[220:223]
	v_mfma_f32_16x16x32_bf16 v[220:223], v[200:203], v[50:53], v[220:223]
	v_mfma_f32_16x16x32_bf16 v[220:223], v[204:207], v[46:49], v[220:223]
	v_mfma_f32_16x16x32_bf16 v[220:223], v[208:211], v[42:45], v[220:223]
	v_mfma_f32_16x16x32_bf16 v[220:223], v[212:215], v[38:41], v[220:223]
	v_mfma_f32_16x16x32_bf16 v[220:223], v[216:219], v[34:37], v[220:223]
	s_nop 7
	v_cvt_pk_bf16_f32 v70, v70, s0
	v_cvt_pk_bf16_f32 v71, v71, s0
	v_cvt_pk_bf16_f32 v72, v72, s0
	v_cvt_pk_bf16_f32 v73, v73, s0
	v_cvt_pk_bf16_f32 v82, v66, s0
	v_cvt_pk_bf16_f32 v83, v67, s0
	v_cvt_pk_bf16_f32 v84, v68, s0
	v_cvt_pk_bf16_f32 v85, v69, s0
	v_lshlrev_b32_e32 v106, 2, v104
	v_cmp_gt_u32_e32 vcc, v106, v102
	v_cvt_pk_bf16_f32 v78, v74, s0
	v_or_b32_e32 v74, 3, v106
	v_cvt_pk_bf16_f32 v79, v75, s0
	s_nop 1
	v_mov_b32_e32 v66, v220
	v_mov_b32_e32 v67, v221
	v_mov_b32_e32 v68, v222
	v_mov_b32_e32 v69, v223
	v_cvt_pk_bf16_f32 v80, v76, s0
	v_cvt_pk_bf16_f32 v81, v77, s0
	v_cmp_gt_u32_e64 s[6:7], v74, v102
	v_cndmask_b32_e64 v75, v82, 0, vcc
	v_or_b32_e32 v120, 51, v106
	s_nop 2
	v_cvt_pk_bf16_f32 v89, v69, s0
	v_or_b32_e32 v69, 2, v106
	v_cvt_pk_bf16_f32 v66, v66, s0
	v_cvt_pk_bf16_f32 v67, v67, s0
	v_cvt_pk_bf16_f32 v68, v68, s0
	v_cmp_lt_u32_e64 s[0:1], v106, v102
	v_cmp_gt_u32_e64 s[4:5], v69, v102
	v_cndmask_b32_e64 v77, v85, 0, s[6:7]
	v_cndmask_b32_e64 v76, 0, v83, s[0:1]
	v_cndmask_b32_e64 v69, v84, 0, s[4:5]
	v_perm_b32 v74, v76, v75, s38
	v_perm_b32 v75, v77, v69, s38
	v_or_b32_e32 v69, 17, v106
	v_or_b32_e32 v76, 16, v106
	v_cmp_gt_u32_e64 s[8:9], v76, v102
	v_cmp_gt_u32_e64 s[10:11], v69, v102
	s_nop 0
	v_cndmask_b32_e64 v70, v70, 0, s[8:9]
	v_cndmask_b32_e64 v69, v71, 0, s[10:11]
	v_perm_b32 v76, v69, v70, s38
	v_or_b32_e32 v69, 19, v106
	v_or_b32_e32 v70, 18, v106
	v_cmp_gt_u32_e64 s[16:17], v70, v102
	v_cmp_gt_u32_e64 s[20:21], v69, v102
	v_or_b32_e32 v71, 35, v106
	v_cndmask_b32_e64 v70, v72, 0, s[16:17]
	v_cndmask_b32_e64 v69, v73, 0, s[20:21]
	v_perm_b32 v77, v69, v70, s38
	v_or_b32_e32 v69, 33, v106
	v_or_b32_e32 v70, 34, v106
	v_or_b32_e32 v72, 32, v106
	v_cmp_gt_u32_e64 s[12:13], v72, v102
	v_cmp_gt_u32_e64 s[14:15], v69, v102
	v_cmp_gt_u32_e64 s[18:19], v70, v102
	v_cmp_gt_u32_e64 s[22:23], v71, v102
	v_cndmask_b32_e64 v72, v78, 0, s[12:13]
	v_cndmask_b32_e64 v69, v79, 0, s[14:15]
	v_cndmask_b32_e64 v70, v80, 0, s[18:19]
	v_cndmask_b32_e64 v71, v81, 0, s[22:23]
	v_perm_b32 v86, v69, v72, s38
	v_perm_b32 v87, v71, v70, s38
	v_or_b32_e32 v69, 49, v106
	v_or_b32_e32 v70, 48, v106
	v_cmp_gt_u32_e64 s[24:25], v70, v102
	v_cmp_gt_u32_e64 s[26:27], v69, v102
	s_nop 0
	v_cndmask_b32_e64 v66, v66, 0, s[24:25]
	v_cndmask_b32_e64 v67, v67, 0, s[26:27]
	v_perm_b32 v88, v67, v66, s38
	v_or_b32_e32 v66, 50, v106
	v_cmp_gt_u32_e64 s[28:29], v66, v102
	v_lshrrev_b32_e32 v67, 1, v104
	v_bfe_u32 v66, v0, 1, 3
	v_cndmask_b32_e64 v121, v68, 0, s[28:29]
	v_lshrrev_b32_e32 v68, 1, v0
	v_bitop3_b32 v69, v67, v68, 7 bitop3:0x78
	v_and_b32_e32 v111, 8, v68
	v_lshlrev_b32_e32 v109, 4, v69
	v_add3_u32 v70, s30, v111, v112
	v_add_u32_e32 v128, v70, v109
	ds_read2st64_b64 v[90:93], v128 offset1:4
	v_bitop3_b32 v68, v67, v66, 2 bitop3:0x36
	v_lshlrev_b32_e32 v110, 4, v68
	v_bitop3_b32 v71, v67, v66, 4 bitop3:0x36
	v_bitop3_b32 v72, v67, v66, 6 bitop3:0x36
	s_waitcnt lgkmcnt(0)
	v_mov_b32_e32 v82, v90
	v_add_u32_e32 v90, v70, v110
	ds_read2st64_b64 v[66:69], v90 offset1:4
	v_lshlrev_b32_e32 v107, 4, v71
	v_lshlrev_b32_e32 v108, 4, v72
	v_add_u32_e32 v136, v70, v107
	v_add_u32_e32 v140, v70, v108
	ds_read2st64_b64 v[94:97], v136 offset1:4
	ds_read2st64_b64 v[70:73], v140 offset1:4
	v_mov_b32_e32 v83, v91
	s_waitcnt lgkmcnt(0)
	v_mov_b32_e32 v84, v66
	v_mov_b32_e32 v85, v67
	v_mov_b32_e32 v78, v94
	v_mov_b32_e32 v79, v95
	v_mov_b32_e32 v80, v70
	v_mov_b32_e32 v81, v71
	v_mfma_f32_16x16x32_bf16 v[98:101], v[82:85], v[74:77], 0
	v_cmp_gt_u32_e64 s[30:31], v120, v102
	v_mov_b32_e32 v67, v93
	v_mov_b32_e32 v70, v96
	v_cndmask_b32_e64 v66, v89, 0, s[30:31]
	v_perm_b32 v89, v66, v121, s38
	v_mov_b32_e32 v66, v92
	ds_read_b128 v[120:123], v114 offset:32768
	ds_read_b128 v[124:127], v114 offset:40960
	v_mfma_f32_16x16x32_bf16 v[98:101], v[78:81], v[86:89], v[98:101]
	v_mov_b32_e32 v71, v97
	ds_read2st64_b64 v[128:131], v128 offset0:8 offset1:12
	ds_read2st64_b64 v[90:93], v90 offset0:8 offset1:12
	ds_read2st64_b64 v[136:139], v136 offset0:8 offset1:12
	s_waitcnt lgkmcnt(0)
	v_mfma_f32_16x16x32_bf16 v[120:123], v[120:123], v[62:65], v[98:101]
	v_mov_b32_e32 v94, v128
	v_mov_b32_e32 v95, v129
	v_mfma_f32_16x16x32_bf16 v[98:101], v[66:69], v[74:77], 0
	v_mov_b32_e32 v96, v90
	v_mov_b32_e32 v97, v91
	v_mov_b32_e32 v90, v130
	v_mfma_f32_16x16x32_bf16 v[132:135], v[70:73], v[86:89], v[98:101]
	v_mov_b32_e32 v91, v131
	s_nop 2
	ds_read2st64_b64 v[98:101], v140 offset0:8 offset1:12
	v_mfma_f32_16x16x32_bf16 v[124:127], v[124:127], v[62:65], v[132:135]
	ds_read_b128 v[144:147], v114 offset:49152
	ds_read_b128 v[148:151], v114 offset:57344
	ds_read_b128 v[128:131], v115 offset:32768
	v_mov_b32_e32 v132, v136
	v_mov_b32_e32 v133, v137
	s_waitcnt lgkmcnt(0)
	v_mov_b32_e32 v134, v98
	v_mov_b32_e32 v135, v99
	v_mov_b32_e32 v98, v138
	v_mov_b32_e32 v99, v139
	v_mfma_f32_16x16x32_bf16 v[140:143], v[94:97], v[74:77], 0
	v_mfma_f32_16x16x32_bf16 v[74:77], v[90:93], v[74:77], 0
	v_mfma_f32_16x16x32_bf16 v[140:143], v[132:135], v[86:89], v[140:143]
	v_mfma_f32_16x16x32_bf16 v[74:77], v[98:101], v[86:89], v[74:77]
	ds_read_b128 v[86:89], v117 offset:32768
	v_mfma_f32_16x16x32_bf16 v[140:143], v[144:147], v[62:65], v[140:143]
	v_mfma_f32_16x16x32_bf16 v[62:65], v[148:151], v[62:65], v[74:77]
	s_nop 4
	ds_read_b128 v[74:77], v117 offset:40960
	s_waitcnt lgkmcnt(0)
	v_mfma_f32_16x16x32_bf16 v[86:89], v[86:89], v[58:61], v[120:123]
	s_nop 2
	ds_read_b128 v[120:123], v117 offset:49152
	v_mfma_f32_16x16x32_bf16 v[74:77], v[74:77], v[58:61], v[124:127]
	s_nop 2
	ds_read_b128 v[124:127], v117 offset:57344
	s_waitcnt lgkmcnt(0)
	v_mfma_f32_16x16x32_bf16 v[120:123], v[120:123], v[58:61], v[140:143]
	v_mfma_f32_16x16x32_bf16 v[58:61], v[124:127], v[58:61], v[62:65]
	ds_read_b128 v[124:127], v115 offset:49152
	s_nop 1
	ds_read_b128 v[62:65], v115 offset:40960
	s_waitcnt lgkmcnt(0)
	v_mfma_f32_16x16x32_bf16 v[62:65], v[62:65], v[54:57], v[74:77]
	s_nop 2
	ds_read_b128 v[74:77], v115 offset:57344
	v_cndmask_b32_e64 v115, 0, 1.0, s[0:1]
	v_mfma_f32_16x16x32_bf16 v[120:123], v[124:127], v[54:57], v[120:123]
	ds_read_b128 v[124:127], v113 offset:32768
	v_mfma_f32_16x16x32_bf16 v[86:89], v[128:131], v[54:57], v[86:89]
	s_waitcnt lgkmcnt(0)
	v_mfma_f32_16x16x32_bf16 v[54:57], v[74:77], v[54:57], v[58:61]
	s_nop 2
	ds_read_b128 v[58:61], v113 offset:40960
	v_mfma_f32_16x16x32_bf16 v[74:77], v[124:127], v[50:53], v[86:89]
	s_nop 2
	ds_read_b128 v[86:89], v113 offset:49152
	s_waitcnt lgkmcnt(0)
	v_mfma_f32_16x16x32_bf16 v[58:61], v[58:61], v[50:53], v[62:65]
	s_nop 2
	ds_read_b128 v[62:65], v113 offset:57344
	v_mov_b32_e32 v113, 0x3f80
	v_cndmask_b32_e64 v114, v113, 0, vcc
	v_mfma_f32_16x16x32_bf16 v[86:89], v[86:89], v[50:53], v[120:123]
	s_nop 2
	ds_read_b128 v[120:123], v119 offset:32768
	s_waitcnt lgkmcnt(0)
	v_mfma_f32_16x16x32_bf16 v[50:53], v[62:65], v[50:53], v[54:57]
	s_nop 2
	ds_read_b128 v[54:57], v119 offset:40960
	v_mfma_f32_16x16x32_bf16 v[62:65], v[120:123], v[46:49], v[74:77]
	s_nop 2
	ds_read_b128 v[74:77], v119 offset:49152
	s_waitcnt lgkmcnt(0)
	v_mfma_f32_16x16x32_bf16 v[74:77], v[74:77], v[46:49], v[86:89]
	s_nop 2
	ds_read_b128 v[86:89], v118 offset:32768
	v_mfma_f32_16x16x32_bf16 v[54:57], v[54:57], v[46:49], v[58:61]
	s_nop 2
	ds_read_b128 v[58:61], v119 offset:57344
	s_waitcnt lgkmcnt(0)
	v_mfma_f32_16x16x32_bf16 v[46:49], v[58:61], v[46:49], v[50:53]
	s_nop 2
	ds_read_b128 v[50:53], v118 offset:40960
	v_mfma_f32_16x16x32_bf16 v[58:61], v[86:89], v[42:45], v[62:65]
	s_nop 2
	ds_read_b128 v[62:65], v118 offset:49152
	s_waitcnt lgkmcnt(0)
	v_mfma_f32_16x16x32_bf16 v[62:65], v[62:65], v[42:45], v[74:77]
	s_nop 2
	ds_read_b128 v[74:77], v116 offset:32768
	v_mfma_f32_16x16x32_bf16 v[50:53], v[50:53], v[42:45], v[54:57]
	s_nop 2
	ds_read_b128 v[54:57], v118 offset:57344
	s_waitcnt lgkmcnt(0)
	v_mfma_f32_16x16x32_bf16 v[42:45], v[54:57], v[42:45], v[46:49]
	s_nop 2
	ds_read_b128 v[46:49], v116 offset:40960
	ds_read_b128 v[54:57], v116 offset:49152
	ds_read_b128 v[86:89], v116 offset:57344
	v_cndmask_b32_e64 v116, v113, 0, s[4:5]
	v_mfma_f32_16x16x32_bf16 v[58:61], v[74:77], v[38:41], v[58:61]
	s_waitcnt lgkmcnt(0)
	v_mfma_f32_16x16x32_bf16 v[46:49], v[46:49], v[38:41], v[50:53]
	s_nop 2
	ds_read_b128 v[50:53], v1 offset:32768
	ds_read_b128 v[74:77], v1 offset:40960
	v_mfma_f32_16x16x32_bf16 v[54:57], v[54:57], v[38:41], v[62:65]
	v_mfma_f32_16x16x32_bf16 v[38:41], v[86:89], v[38:41], v[42:45]
	v_cndmask_b32_e64 v87, v113, 0, s[12:13]
	s_nop 0
	v_cndmask_b32_e64 v62, 1.0, 0, s[6:7]
	v_cndmask_b32_e64 v63, v113, 0, s[8:9]
	ds_read_b128 v[42:45], v1 offset:49152
	s_waitcnt lgkmcnt(0)
	v_mfma_f32_16x16x32_bf16 v[50:53], v[50:53], v[34:37], v[58:61]
	v_cndmask_b32_e64 v64, 1.0, 0, s[10:11]
	v_cndmask_b32_e64 v65, v113, 0, s[16:17]
	v_cndmask_b32_e64 v86, 1.0, 0, s[20:21]
	ds_read_b128 v[58:61], v1 offset:57344
	v_cndmask_b32_e64 v1, 1.0, 0, s[14:15]
	v_mfma_f32_16x16x32_bf16 v[46:49], v[74:77], v[34:37], v[46:49]
	v_cndmask_b32_e64 v74, v113, 0, s[18:19]
	v_cndmask_b32_e64 v75, 1.0, 0, s[22:23]
	v_cndmask_b32_e64 v76, v113, 0, s[24:25]
	v_mfma_f32_16x16x32_bf16 v[42:45], v[42:45], v[34:37], v[54:57]
	v_cndmask_b32_e64 v77, 1.0, 0, s[26:27]
	v_cndmask_b32_e64 v88, v113, 0, s[28:29]
	v_cndmask_b32_e64 v89, 1.0, 0, s[30:31]
	s_waitcnt lgkmcnt(0)
	v_mfma_f32_16x16x32_bf16 v[38:41], v[58:61], v[34:37], v[38:41]
	v_or_b32_e32 v34, v1, v87
	v_add3_u32 v1, s34, v111, v112
	v_add_u32_e32 v113, v1, v109
	v_add_u32_e32 v118, v1, v110
	v_or_b32_e32 v55, v62, v116
	v_or_b32_e32 v56, v64, v63
	v_or_b32_e32 v57, v86, v65
	v_or_b32_e32 v35, v75, v74
	ds_read2st64_b64 v[62:65], v113 offset1:4
	v_or_b32_e32 v36, v77, v76
	ds_read2st64_b64 v[74:77], v118 offset1:4
	v_add_u32_e32 v119, v1, v107
	v_add_u32_e32 v1, v1, v108
	v_or_b32_e32 v54, v115, v114
	v_or_b32_e32 v37, v89, v88
	ds_read2st64_b64 v[86:89], v119 offset1:4
	ds_read2st64_b64 v[114:117], v1 offset1:4
	v_mfma_f32_16x16x32_bf16 v[58:61], v[82:85], v[54:57], 0
	s_waitcnt lgkmcnt(0)
	v_mov_b32_e32 v82, v62
	v_mov_b32_e32 v83, v63
	v_mov_b32_e32 v84, v74
	v_mov_b32_e32 v85, v75
	v_mfma_f32_16x16x32_bf16 v[66:69], v[66:69], v[54:57], 0
	v_mov_b32_e32 v74, v64
	v_mov_b32_e32 v75, v65
	ds_read2st64_b64 v[62:65], v113 offset0:8 offset1:12
	v_mfma_f32_16x16x32_bf16 v[58:61], v[78:81], v[34:37], v[58:61]
	v_mov_b32_e32 v78, v86
	v_mov_b32_e32 v79, v87
	v_mov_b32_e32 v80, v114
	v_mov_b32_e32 v81, v115
	v_mfma_f32_16x16x32_bf16 v[82:85], v[82:85], v[54:57], 0
	v_mov_b32_e32 v114, v88
	v_mov_b32_e32 v115, v89
	v_mul_f32_e32 v51, 0x3d800000, v51
	v_mfma_f32_16x16x32_bf16 v[66:69], v[70:73], v[34:37], v[66:69]
	v_mul_f32_e32 v52, 0x3d800000, v52
	v_mul_f32_e32 v53, 0x3d800000, v53
	s_mov_b32 s34, 0xff61b1e6
	v_mfma_f32_16x16x32_bf16 v[70:73], v[94:97], v[54:57], 0
	v_mul_f32_e32 v46, 0x3d800000, v46
	s_nop 2
	v_add_f32_e32 v86, v66, v26
	v_add_f32_e32 v87, v67, v27
	v_mfma_f32_16x16x32_bf16 v[78:81], v[78:81], v[34:37], v[82:85]
	v_add_f32_e32 v94, v68, v28
	v_add_f32_e32 v95, v69, v29
	ds_read2st64_b64 v[66:69], v119 offset0:8 offset1:12
	v_add_f32_e32 v82, v58, v30
	v_add_f32_e32 v83, v59, v31
	v_add_f32_e32 v84, v60, v32
	v_add_f32_e32 v85, v61, v33
	v_mfma_f32_16x16x32_bf16 v[30:33], v[132:135], v[34:37], v[70:73]
	v_mul_f32_e32 v47, 0x3d800000, v47
	v_mul_f32_e32 v48, 0x3d800000, v48
	v_mul_f32_e32 v49, 0x3d800000, v49
	v_mfma_f32_16x16x32_bf16 v[26:29], v[90:93], v[54:57], 0
	ds_read2st64_b64 v[70:73], v1 offset0:8 offset1:12
	s_nop 2
	v_add_f32_e32 v90, v30, v22
	v_add_f32_e32 v91, v31, v23
	v_add_f32_e32 v92, v32, v24
	v_add_f32_e32 v88, v33, v25
	ds_read2st64_b64 v[22:25], v118 offset0:8 offset1:12
	v_mfma_f32_16x16x32_bf16 v[58:61], v[74:77], v[54:57], 0
	s_waitcnt lgkmcnt(0)
	v_mov_b32_e32 v74, v66
	v_mov_b32_e32 v75, v67
	v_mov_b32_e32 v76, v70
	v_mfma_f32_16x16x32_bf16 v[30:33], v[114:117], v[34:37], v[58:61]
	v_mov_b32_e32 v77, v71
	v_mov_b32_e32 v70, v68
	v_add_f32_e32 v68, v79, v15
	v_mov_b32_e32 v58, v62
	v_mov_b32_e32 v59, v63
	v_mov_b32_e32 v60, v22
	v_mov_b32_e32 v61, v23
	v_mfma_f32_16x16x32_bf16 v[26:29], v[98:101], v[34:37], v[26:29]
	v_rcp_f32_e32 v62, v85
	v_rcp_f32_e32 v63, v86
	v_rcp_f32_e32 v79, v87
	v_mfma_f32_16x16x32_bf16 v[58:61], v[58:61], v[54:57], 0
	v_mov_b32_e32 v71, v69
	s_nop 2
	v_add_f32_e32 v26, v26, v18
	v_add_f32_e32 v1, v27, v19
	v_add_f32_e32 v27, v28, v20
	v_add_f32_e32 v28, v29, v21
	v_mfma_f32_16x16x32_bf16 v[18:21], v[74:77], v[34:37], v[58:61]
	v_mul_f32_e32 v29, 0x3d800000, v50
	v_rcp_f32_e32 v50, v82
	v_add_f32_e32 v69, v80, v16
	v_rcp_f32_e32 v60, v83
	v_rcp_f32_e32 v61, v84
	v_add_f32_e32 v74, v81, v17
	v_rcp_f32_e32 v80, v94
	v_rcp_f32_e32 v81, v95
	v_add_f32_e32 v75, v30, v10
	v_add_f32_e32 v76, v31, v11
	v_mul_f32_e32 v30, 0x3d800000, v42
	v_mul_f32_e32 v31, 0x3d800000, v43
	v_add_f32_e32 v42, v18, v6
	v_add_f32_e32 v43, v19, v7
	v_mul_f32_e32 v18, v29, v50
	v_mul_f32_e32 v19, v51, v60
	v_rcp_f32_e32 v82, v90
	v_rcp_f32_e32 v83, v91
	v_add_f32_e32 v77, v32, v12
	v_mul_f32_e32 v32, 0x3d800000, v44
	v_add_f32_e32 v44, v20, v8
	v_max3_f32 v18, v18, s34, v19
	v_mul_f32_e32 v19, v52, v61
	v_mul_f32_e32 v20, v53, v62
	v_rcp_f32_e32 v84, v92
	v_rcp_f32_e32 v85, v88
	v_max3_f32 v18, v18, v19, v20
	v_mul_f32_e32 v19, v46, v63
	v_mul_f32_e32 v20, v47, v79
	v_rcp_f32_e32 v86, v26
	v_rcp_f32_e32 v87, v1
	v_max3_f32 v18, v18, v19, v20
	v_mul_f32_e32 v19, v48, v80
	v_mul_f32_e32 v20, v49, v81
	v_rcp_f32_e32 v88, v27
	v_rcp_f32_e32 v89, v28
	v_add_f32_e32 v67, v78, v14
	v_add_f32_e32 v78, v33, v13
	v_mul_f32_e32 v33, 0x3d800000, v45
	v_max3_f32 v18, v18, v19, v20
	v_mul_f32_e32 v19, v30, v82
	v_mul_f32_e32 v20, v31, v83
	v_max3_f32 v18, v18, v19, v20
	v_mul_f32_e32 v19, v32, v84
	v_mul_f32_e32 v20, v33, v85
	v_mul_f32_e32 v38, 0x3d800000, v38
	v_mul_f32_e32 v39, 0x3d800000, v39
	v_max3_f32 v18, v18, v19, v20
	v_mul_f32_e32 v1, v38, v86
	v_mul_f32_e32 v19, v39, v87
	v_mul_f32_e32 v40, 0x3d800000, v40
	v_mul_f32_e32 v41, 0x3d800000, v41
	v_max3_f32 v1, v18, v1, v19
	v_mul_f32_e32 v18, v40, v88
	v_mul_f32_e32 v19, v41, v89
	v_max3_f32 v1, v1, v18, v19
	v_mbcnt_lo_u32_b32 v18, -1, 0
	v_mbcnt_hi_u32_b32 v26, -1, v18
	v_and_b32_e32 v19, 64, v26
	v_xor_b32_e32 v18, 16, v26
	v_add_u32_e32 v27, 64, v19
	v_cmp_lt_i32_e64 s[34:35], v18, v27
	v_mov_b32_e32 v22, v64
	v_mov_b32_e32 v23, v65
	v_cndmask_b32_e64 v18, v26, v18, s[34:35]
	v_lshlrev_b32_e32 v64, 2, v18
	ds_bpermute_b32 v28, v64, v1
	v_add_f32_e32 v45, v21, v9
	v_mfma_f32_16x16x32_bf16 v[18:21], v[22:25], v[54:57], 0
	v_lshlrev_b32_e32 v58, 9, v102
	v_mov_b32_e32 v59, 0
	s_waitcnt lgkmcnt(0)
	v_max_f32_e32 v24, v28, v28
	v_max_f32_e32 v24, v1, v24
	v_xor_b32_e32 v1, 32, v26
	v_cmp_lt_i32_e64 s[34:35], v1, v27
	v_lshl_add_u64 v[22:23], s[36:37], 0, v[58:59]
	v_lshlrev_b32_e32 v58, 3, v104
	v_cndmask_b32_e64 v1, v26, v1, s[34:35]
	v_lshlrev_b32_e32 v65, 2, v1
	ds_bpermute_b32 v25, v65, v24
	v_lshl_add_u64 v[22:23], v[22:23], 0, v[58:59]
	v_and_b32_e32 v58, 0x100, v0
	v_lshrrev_b32_e32 v66, 8, v0
	v_lshl_add_u64 v[0:1], v[22:23], 0, v[58:59]
	s_waitcnt lgkmcnt(0)
	v_max_f32_e32 v22, v25, v25
	v_max_f32_e32 v54, v24, v22
	v_fma_f32 v22, v29, v50, -v54
	v_mul_f32_e32 v22, 0x3fb8aa3b, v22
	v_fma_f32 v23, v51, v60, -v54
	v_exp_f32_e32 v22, v22
	v_mul_f32_e32 v23, 0x3fb8aa3b, v23
	v_fma_f32 v24, v52, v61, -v54
	v_exp_f32_e32 v23, v23
	v_mul_f32_e32 v24, 0x3fb8aa3b, v24
	v_fma_f32 v25, v53, v62, -v54
	v_exp_f32_e32 v24, v24
	v_mul_f32_e32 v25, 0x3fb8aa3b, v25
	v_fma_f32 v26, v46, v63, -v54
	v_exp_f32_e32 v25, v25
	v_mul_f32_e32 v26, 0x3fb8aa3b, v26
	v_fma_f32 v27, v47, v79, -v54
	v_exp_f32_e32 v26, v26
	v_mul_f32_e32 v27, 0x3fb8aa3b, v27
	v_fma_f32 v28, v48, v80, -v54
	v_add_f32_e32 v46, 0, v22
	v_exp_f32_e32 v27, v27
	v_mul_f32_e32 v28, 0x3fb8aa3b, v28
	v_fma_f32 v29, v49, v81, -v54
	v_add_f32_e32 v46, v46, v23
	v_exp_f32_e32 v28, v28
	v_mul_f32_e32 v29, 0x3fb8aa3b, v29
	v_add_f32_e32 v46, v46, v24
	v_fma_f32 v30, v30, v82, -v54
	v_exp_f32_e32 v29, v29
	v_add_f32_e32 v46, v46, v25
	v_mul_f32_e32 v30, 0x3fb8aa3b, v30
	v_fma_f32 v31, v31, v83, -v54
	v_add_f32_e32 v46, v46, v26
	v_exp_f32_e32 v30, v30
	v_mul_f32_e32 v31, 0x3fb8aa3b, v31
	v_fma_f32 v32, v32, v84, -v54
	v_add_f32_e32 v46, v46, v27
	v_exp_f32_e32 v31, v31
	v_mul_f32_e32 v32, 0x3fb8aa3b, v32
	v_fma_f32 v33, v33, v85, -v54
	v_add_f32_e32 v46, v46, v28
	v_exp_f32_e32 v32, v32
	v_mul_f32_e32 v33, 0x3fb8aa3b, v33
	v_fma_f32 v38, v38, v86, -v54
	v_add_f32_e32 v46, v46, v29
	v_exp_f32_e32 v33, v33
	v_mul_f32_e32 v38, 0x3fb8aa3b, v38
	v_fma_f32 v39, v39, v87, -v54
	v_add_f32_e32 v46, v46, v30
	v_exp_f32_e32 v38, v38
	v_mul_f32_e32 v39, 0x3fb8aa3b, v39
	v_fma_f32 v40, v40, v88, -v54
	v_add_f32_e32 v46, v46, v31
	v_exp_f32_e32 v39, v39
	v_mul_f32_e32 v40, 0x3fb8aa3b, v40
	v_fma_f32 v41, v41, v89, -v54
	v_add_f32_e32 v46, v46, v32
	v_exp_f32_e32 v40, v40
	v_mul_f32_e32 v41, 0x3fb8aa3b, v41
	v_add_f32_e32 v46, v46, v33
	v_exp_f32_e32 v41, v41
	v_add_f32_e32 v46, v46, v38
	v_add_f32_e32 v46, v46, v39
	v_add_f32_e32 v46, v46, v40
	v_add_f32_e32 v58, v46, v41
	ds_bpermute_b32 v79, v64, v58
	global_load_dwordx2 v[62:63], v[0:1], off
	global_load_dwordx2 v[60:61], v[0:1], off offset:32
	global_load_dwordx2 v[56:57], v[0:1], off offset:64
	global_load_dwordx2 v[52:53], v[0:1], off offset:96
	global_load_dwordx2 v[54:55], v[0:1], off offset:128
	global_load_dwordx2 v[50:51], v[0:1], off offset:160
	global_load_dwordx2 v[48:49], v[0:1], off offset:192
	global_load_dwordx2 v[46:47], v[0:1], off offset:224
	v_mfma_f32_16x16x32_bf16 v[18:21], v[70:73], v[34:37], v[18:21]
	v_rcp_f32_e32 v34, v75
	s_waitcnt lgkmcnt(0)
	v_add_f32_e32 v0, v58, v79
	ds_bpermute_b32 v1, v65, v0
	v_rcp_f32_e32 v35, v76
	v_rcp_f32_e32 v36, v77
	s_nop 1
	v_add_f32_e32 v58, v18, v2
	v_rcp_f32_e32 v18, v67
	s_waitcnt lgkmcnt(0)
	v_add_f32_e32 v0, v0, v1
	v_rcp_f32_e32 v0, v0
	v_add_f32_e32 v1, v19, v3
	v_rcp_f32_e32 v19, v68
	v_add_f32_e32 v70, v20, v4
	v_add_f32_e32 v71, v21, v5
	v_rcp_f32_e32 v20, v69
	v_rcp_f32_e32 v21, v74
	v_mul_f32_e32 v0, 0x43800000, v0
	v_pk_mul_f32 v[22:23], v[0:1], v[22:23] op_sel_hi:[0,1]
	v_pk_mul_f32 v[18:19], v[22:23], v[18:19]
	v_pk_mul_f32 v[22:23], v[0:1], v[24:25] op_sel_hi:[0,1]
	v_pk_mul_f32 v[20:21], v[22:23], v[20:21]
	v_rcp_f32_e32 v37, v78
	v_pk_mul_f32 v[14:15], v[14:15], v[18:19]
	v_pk_mul_f32 v[16:17], v[16:17], v[20:21]
	v_cvt_pk_f16_f32 v14, v14, v15
	v_cvt_pk_f16_f32 v15, v16, v17
	v_pk_mul_f32 v[16:17], v[0:1], v[26:27] op_sel_hi:[0,1]
	v_pk_mul_f32 v[16:17], v[16:17], v[34:35]
	v_cvt_pk_bf16_f32 v18, v18, v19
	v_cvt_pk_bf16_f32 v19, v20, v21
	v_pk_mul_f32 v[10:11], v[10:11], v[16:17]
	v_cvt_pk_bf16_f32 v20, v16, v17
	v_pk_mul_f32 v[16:17], v[0:1], v[28:29] op_sel_hi:[0,1]
	v_pk_mul_f32 v[72:73], v[16:17], v[36:37]
	v_rcp_f32_e32 v16, v42
	v_rcp_f32_e32 v17, v43
	v_rcp_f32_e32 v24, v44
	v_rcp_f32_e32 v25, v45
	v_rcp_f32_e32 v26, v58
	v_rcp_f32_e32 v27, v1
	v_pk_mul_f32 v[22:23], v[0:1], v[30:31] op_sel_hi:[0,1]
	v_pk_mul_f32 v[76:77], v[22:23], v[16:17]
	v_pk_mul_f32 v[16:17], v[0:1], v[32:33] op_sel_hi:[0,1]
	v_pk_mul_f32 v[78:79], v[16:17], v[24:25]
	v_pk_mul_f32 v[16:17], v[0:1], v[38:39] op_sel_hi:[0,1]
	s_add_i32 s34, 0, 0x24000
	v_pk_mul_f32 v[80:81], v[16:17], v[26:27]
	v_add3_u32 v16, s34, v112, v111
	v_add_u32_e32 v17, v16, v109
	v_add_u32_e32 v58, v16, v110
	s_barrier
	ds_write_b128 v152, v[70:73]
	ds_write_b128 v152, v[76:79] offset:1024
	ds_write_b64 v153, v[0:1] offset:2048
	ds_write_b64 v153, v[10:11] offset:2560
	ds_write_b64 v153, v[14:15] offset:3072
	ds_write_b64 v153, v[18:19] offset:3584
	ds_write_b64 v153, v[40:41] offset:4096
	ds_write_b64 v153, v[80:81] offset:4608
	ds_write_b32 v154, v20 offset:5120
	s_waitcnt lgkmcnt(0)
	s_branch .Lat_join

	.amdhsa_kernel _Z9attn_fastPKtS0_S0_S0_S0_S0_S0_S0_S0_PKfS2_Pt
		.amdhsa_group_segment_fixed_size 0
		.amdhsa_private_segment_fixed_size 0
		.amdhsa_kernarg_size 96
		.amdhsa_user_sgpr_count 2
		.amdhsa_user_sgpr_dispatch_ptr 0
		.amdhsa_user_sgpr_queue_ptr 0
		.amdhsa_user_sgpr_kernarg_segment_ptr 1
		.amdhsa_user_sgpr_dispatch_id 0
		.amdhsa_user_sgpr_kernarg_preload_length 0
		.amdhsa_user_sgpr_kernarg_preload_offset 0
		.amdhsa_user_sgpr_private_segment_size 0
		.amdhsa_uses_dynamic_stack 0
		.amdhsa_enable_private_segment 0
		.amdhsa_system_sgpr_workgroup_id_x 1
		.amdhsa_system_sgpr_workgroup_id_y 0
		.amdhsa_system_sgpr_workgroup_id_z 0
		.amdhsa_system_sgpr_workgroup_info 0
		.amdhsa_system_vgpr_workitem_id 0
		.amdhsa_next_free_vgpr 224
		.amdhsa_next_free_sgpr 46
		.amdhsa_accum_offset 224
		.amdhsa_reserve_vcc 1
		.amdhsa_float_round_mode_32 0
		.amdhsa_float_round_mode_16_64 0
		.amdhsa_float_denorm_mode_32 3
		.amdhsa_float_denorm_mode_16_64 3
		.amdhsa_dx10_clamp 1
		.amdhsa_ieee_mode 1
		.amdhsa_fp16_overflow 0
		.amdhsa_tg_split 0
		.amdhsa_exception_fp_ieee_invalid_op 0
		.amdhsa_exception_fp_denorm_src 0
		.amdhsa_exception_fp_ieee_div_zero 0
		.amdhsa_exception_fp_ieee_overflow 0
		.amdhsa_exception_fp_ieee_underflow 0
		.amdhsa_exception_fp_ieee_inexact 0
		.amdhsa_exception_int_div_zero 0
	.end_amdhsa_kernel

amdhsa.kernels:
  - .agpr_count:     0
    .args:
      - .actual_access:  read_only
        .address_space:  global
        .offset:         0
        .size:           8
        .value_kind:     global_buffer
      - .actual_access:  read_only
        .address_space:  global
        .offset:         8
        .size:           8
        .value_kind:     global_buffer
      - .actual_access:  write_only
        .address_space:  global
        .offset:         16
        .size:           8
        .value_kind:     global_buffer
      - .offset:         24
        .size:           4
        .value_kind:     by_value
      - .offset:         28
        .size:           4
        .value_kind:     by_value
      - .offset:         32
        .size:           4
        .value_kind:     by_value
      - .offset:         36
        .size:           4
        .value_kind:     by_value
    .group_segment_fixed_size: 8256
    .kernarg_segment_align: 8
    .kernarg_segment_size: 40
    .language:       OpenCL C
    .language_version:
      - 2
      - 0
    .max_flat_workgroup_size: 256
    .name:           _Z14gemm_f32_naivePKfS0_Pfiiii
    .private_segment_fixed_size: 0
    .sgpr_count:     24
    .sgpr_spill_count: 0
    .symbol:         _Z14gemm_f32_naivePKfS0_Pfiiii.kd
    .uniform_work_group_size: 1
    .uses_dynamic_stack: false
    .vgpr_count:     76
    .vgpr_spill_count: 0
    .wavefront_size: 64
  - .agpr_count:     0
    .args:
      - .actual_access:  read_only
        .address_space:  global
        .offset:         0
        .size:           8
        .value_kind:     global_buffer
      - .actual_access:  write_only
        .address_space:  global
        .offset:         8
        .size:           8
        .value_kind:     global_buffer
      - .actual_access:  write_only
        .address_space:  global
        .offset:         16
        .size:           8
        .value_kind:     global_buffer
      - .actual_access:  write_only
        .address_space:  global
        .offset:         24
        .size:           8
        .value_kind:     global_buffer
      - .actual_access:  write_only
        .address_space:  global
        .offset:         32
        .size:           8
        .value_kind:     global_buffer
      - .actual_access:  write_only
        .address_space:  global
        .offset:         40
        .size:           8
        .value_kind:     global_buffer
      - .actual_access:  write_only
        .address_space:  global
        .offset:         48
        .size:           8
        .value_kind:     global_buffer
    .group_segment_fixed_size: 0
    .kernarg_segment_align: 8
    .kernarg_segment_size: 56
    .language:       OpenCL C
    .language_version:
      - 2
      - 0
    .max_flat_workgroup_size: 256
    .name:           _Z10post_naivePKfPtS1_S1_S1_S1_S1_
    .private_segment_fixed_size: 0
    .sgpr_count:     28
    .sgpr_spill_count: 0
    .symbol:         _Z10post_naivePKfPtS1_S1_S1_S1_S1_.kd
    .uniform_work_group_size: 1
    .uses_dynamic_stack: false
    .vgpr_count:     38
    .vgpr_spill_count: 0
    .wavefront_size: 64
  - .agpr_count:     0
    .args:
      - .actual_access:  read_only
        .address_space:  global
        .offset:         0
        .size:           8
        .value_kind:     global_buffer
      - .actual_access:  read_only
        .address_space:  global
        .offset:         8
        .size:           8
        .value_kind:     global_buffer
      - .actual_access:  read_only
        .address_space:  global
        .offset:         16
        .size:           8
        .value_kind:     global_buffer
      - .actual_access:  read_only
        .address_space:  global
        .offset:         24
        .size:           8
        .value_kind:     global_buffer
      - .actual_access:  read_only
        .address_space:  global
        .offset:         32
        .size:           8
        .value_kind:     global_buffer
      - .actual_access:  read_only
        .address_space:  global
        .offset:         40
        .size:           8
        .value_kind:     global_buffer
      - .actual_access:  read_only
        .address_space:  global
        .offset:         48
        .size:           8
        .value_kind:     global_buffer
      - .actual_access:  write_only
        .address_space:  global
        .offset:         56
        .size:           8
        .value_kind:     global_buffer
      - .actual_access:  write_only
        .address_space:  global
        .offset:         64
        .size:           8
        .value_kind:     global_buffer
      - .actual_access:  write_only
        .address_space:  global
        .offset:         72
        .size:           8
        .value_kind:     global_buffer
      - .actual_access:  write_only
        .address_space:  global
        .offset:         80
        .size:           8
        .value_kind:     global_buffer
    .group_segment_fixed_size: 1152
    .kernarg_segment_align: 8
    .kernarg_segment_size: 88
    .language:       OpenCL C
    .language_version:
      - 2
      - 0
    .max_flat_workgroup_size: 256
    .name:           _Z11gates_naivePKfS0_S0_S0_S0_S0_S0_PtS1_S1_S1_
    .private_segment_fixed_size: 0
    .sgpr_count:     32
    .sgpr_spill_count: 0
    .symbol:         _Z11gates_naivePKfS0_S0_S0_S0_S0_S0_PtS1_S1_S1_.kd
    .uniform_work_group_size: 1
    .uses_dynamic_stack: false
    .vgpr_count:     66
    .vgpr_spill_count: 0
    .wavefront_size: 64
  - .agpr_count:     0
    .args:
      - .actual_access:  read_only
        .address_space:  global
        .offset:         0
        .size:           8
        .value_kind:     global_buffer
      - .actual_access:  read_only
        .address_space:  global
        .offset:         8
        .size:           8
        .value_kind:     global_buffer
      - .actual_access:  read_only
        .address_space:  global
        .offset:         16
        .size:           8
        .value_kind:     global_buffer
      - .actual_access:  read_only
        .address_space:  global
        .offset:         24
        .size:           8
        .value_kind:     global_buffer
      - .actual_access:  read_only
        .address_space:  global
        .offset:         32
        .size:           8
        .value_kind:     global_buffer
      - .actual_access:  read_only
        .address_space:  global
        .offset:         40
        .size:           8
        .value_kind:     global_buffer
      - .actual_access:  read_only
        .address_space:  global
        .offset:         48
        .size:           8
        .value_kind:     global_buffer
      - .actual_access:  write_only
        .address_space:  global
        .offset:         56
        .size:           8
        .value_kind:     global_buffer
    .group_segment_fixed_size: 12560
    .kernarg_segment_align: 8
    .kernarg_segment_size: 64
    .language:       OpenCL C
    .language_version:
      - 2
      - 0
    .max_flat_workgroup_size: 256
    .name:           _Z10attn_naivePKtS0_S0_S0_S0_S0_PKfPf
    .private_segment_fixed_size: 0
    .sgpr_count:     33
    .sgpr_spill_count: 0
    .symbol:         _Z10attn_naivePKtS0_S0_S0_S0_S0_PKfPf.kd
    .uniform_work_group_size: 1
    .uses_dynamic_stack: false
    .vgpr_count:     82
    .vgpr_spill_count: 0
    .wavefront_size: 64
  - .agpr_count:     0
    .args:
      - .address_space:  global
        .offset:         0
        .size:           8
        .value_kind:     global_buffer
      - .address_space:  global
        .offset:         8
        .size:           8
        .value_kind:     global_buffer
      - .actual_access:  write_only
        .address_space:  global
        .offset:         16
        .size:           8
        .value_kind:     global_buffer
    .group_segment_fixed_size: 0
    .kernarg_segment_align: 8
    .kernarg_segment_size: 24
    .language:       OpenCL C
    .language_version:
      - 2
      - 0
    .max_flat_workgroup_size: 512
    .name:           _Z8gemm_outPKtS0_Pf
    .private_segment_fixed_size: 0
    .sgpr_count:     26
    .sgpr_spill_count: 0
    .symbol:         _Z8gemm_outPKtS0_Pf.kd
    .uniform_work_group_size: 1
    .uses_dynamic_stack: false
    .vgpr_count:     158
    .vgpr_spill_count: 0
    .wavefront_size: 64
  - .agpr_count:     0
    .args:
      - .address_space:  global
        .offset:         0
        .size:           8
        .value_kind:     global_buffer
      - .address_space:  global
        .offset:         8
        .size:           8
        .value_kind:     global_buffer
      - .actual_access:  write_only
        .address_space:  global
        .offset:         16
        .size:           8
        .value_kind:     global_buffer
    .group_segment_fixed_size: 0
    .kernarg_segment_align: 8
    .kernarg_segment_size: 24
    .language:       OpenCL C
    .language_version:
      - 2
      - 0
    .max_flat_workgroup_size: 512
    .name:           _Z9gemm_out2PKtS0_Pf
    .private_segment_fixed_size: 0
    .sgpr_count:     27
    .sgpr_spill_count: 0
    .symbol:         _Z9gemm_out2PKtS0_Pf.kd
    .uniform_work_group_size: 1
    .uses_dynamic_stack: false
    .vgpr_count:     146
    .vgpr_spill_count: 0
    .wavefront_size: 64
  - .agpr_count:     0
    .args:
      - .actual_access:  read_only
        .address_space:  global
        .offset:         0
        .size:           8
        .value_kind:     global_buffer
      - .actual_access:  write_only
        .address_space:  global
        .offset:         8
        .size:           8
        .value_kind:     global_buffer
    .group_segment_fixed_size: 0
    .kernarg_segment_align: 8
    .kernarg_segment_size: 16
    .language:       OpenCL C
    .language_version:
      - 2
      - 0
    .max_flat_workgroup_size: 256
    .name:           _Z6conv_xPKfPt
    .private_segment_fixed_size: 0
    .sgpr_count:     14
    .sgpr_spill_count: 0
    .symbol:         _Z6conv_xPKfPt.kd
    .uniform_work_group_size: 1
    .uses_dynamic_stack: false
    .vgpr_count:     12
    .vgpr_spill_count: 0
    .wavefront_size: 64
  - .agpr_count:     0
    .args:
      - .actual_access:  read_only
        .address_space:  global
        .offset:         0
        .size:           8
        .value_kind:     global_buffer
      - .actual_access:  read_only
        .address_space:  global
        .offset:         8
        .size:           8
        .value_kind:     global_buffer
      - .actual_access:  read_only
        .address_space:  global
        .offset:         16
        .size:           8
        .value_kind:     global_buffer
      - .actual_access:  read_only
        .address_space:  global
        .offset:         24
        .size:           8
        .value_kind:     global_buffer
      - .actual_access:  read_only
        .address_space:  global
        .offset:         32
        .size:           8
        .value_kind:     global_buffer
      - .actual_access:  write_only
        .address_space:  global
        .offset:         40
        .size:           8
        .value_kind:     global_buffer
      - .actual_access:  write_only
        .address_space:  global
        .offset:         48
        .size:           8
        .value_kind:     global_buffer
    .group_segment_fixed_size: 16640
    .kernarg_segment_align: 8
    .kernarg_segment_size: 56
    .language:       OpenCL C
    .language_version:
      - 2
      - 0
    .max_flat_workgroup_size: 256
    .name:           _Z7conv_wTPKfS0_S0_S0_S0_PtS1_
    .private_segment_fixed_size: 0
    .sgpr_count:     26
    .sgpr_spill_count: 0
    .symbol:         _Z7conv_wTPKfS0_S0_S0_S0_PtS1_.kd
    .uniform_work_group_size: 1
    .uses_dynamic_stack: false
    .vgpr_count:     51
    .vgpr_spill_count: 0
    .wavefront_size: 64
  - .agpr_count:     0
    .args:
      - .actual_access:  read_only
        .address_space:  global
        .offset:         0
        .size:           8
        .value_kind:     global_buffer
      - .actual_access:  read_only
        .address_space:  global
        .offset:         8
        .size:           8
        .value_kind:     global_buffer
      - .actual_access:  write_only
        .address_space:  global
        .offset:         16
        .size:           8
        .value_kind:     global_buffer
    .group_segment_fixed_size: 0
    .kernarg_segment_align: 8
    .kernarg_segment_size: 24
    .language:       OpenCL C
    .language_version:
      - 2
      - 0
    .max_flat_workgroup_size: 256
    .name:           _Z7conv_w1PKfS0_Pt
    .private_segment_fixed_size: 0
    .sgpr_count:     16
    .sgpr_spill_count: 0
    .symbol:         _Z7conv_w1PKfS0_Pt.kd
    .uniform_work_group_size: 1
    .uses_dynamic_stack: false
    .vgpr_count:     6
    .vgpr_spill_count: 0
    .wavefront_size: 64
  - .agpr_count:     8
    .args:
      - .actual_access:  read_only
        .address_space:  global
        .offset:         0
        .size:           8
        .value_kind:     global_buffer
      - .actual_access:  read_only
        .address_space:  global
        .offset:         8
        .size:           8
        .value_kind:     global_buffer
      - .actual_access:  read_only
        .address_space:  global
        .offset:         16
        .size:           8
        .value_kind:     global_buffer
      - .actual_access:  read_only
        .address_space:  global
        .offset:         24
        .size:           8
        .value_kind:     global_buffer
      - .actual_access:  read_only
        .address_space:  global
        .offset:         32
        .size:           8
        .value_kind:     global_buffer
      - .actual_access:  read_only
        .address_space:  global
        .offset:         40
        .size:           8
        .value_kind:     global_buffer
      - .actual_access:  write_only
        .address_space:  global
        .offset:         48
        .size:           8
        .value_kind:     global_buffer
      - .actual_access:  write_only
        .address_space:  global
        .offset:         56
        .size:           8
        .value_kind:     global_buffer
      - .actual_access:  write_only
        .address_space:  global
        .offset:         64
        .size:           8
        .value_kind:     global_buffer
    .group_segment_fixed_size: 10240
    .kernarg_segment_align: 8
    .kernarg_segment_size: 72
    .language:       OpenCL C
    .language_version:
      - 2
      - 0
    .max_flat_workgroup_size: 256
    .name:           _Z10gates_fastPKtS0_PKfS2_S2_S2_PtS3_S3_
    .private_segment_fixed_size: 0
    .sgpr_count:     24
    .sgpr_spill_count: 0
    .symbol:         _Z10gates_fastPKtS0_PKfS2_S2_S2_PtS3_S3_.kd
    .uniform_work_group_size: 1
    .uses_dynamic_stack: false
    .vgpr_count:     96
    .vgpr_spill_count: 0
    .wavefront_size: 64
  - .agpr_count:     4
    .args:
      - .actual_access:  read_only
        .address_space:  global
        .offset:         0
        .size:           8
        .value_kind:     global_buffer
      - .actual_access:  read_only
        .address_space:  global
        .offset:         8
        .size:           8
        .value_kind:     global_buffer
      - .actual_access:  read_only
        .address_space:  global
        .offset:         16
        .size:           8
        .value_kind:     global_buffer
      - .actual_access:  read_only
        .address_space:  global
        .offset:         24
        .size:           8
        .value_kind:     global_buffer
      - .actual_access:  write_only
        .address_space:  global
        .offset:         32
        .size:           8
        .value_kind:     global_buffer
      - .actual_access:  write_only
        .address_space:  global
        .offset:         40
        .size:           8
        .value_kind:     global_buffer
      - .actual_access:  write_only
        .address_space:  global
        .offset:         48
        .size:           8
        .value_kind:     global_buffer
    .group_segment_fixed_size: 0
    .kernarg_segment_align: 8
    .kernarg_segment_size: 56
    .language:       OpenCL C
    .language_version:
      - 2
      - 0
    .max_flat_workgroup_size: 256
    .name:           _Z10state_fastPKtS0_S0_S0_PtS1_Pf
    .private_segment_fixed_size: 0
    .sgpr_count:     20
    .sgpr_spill_count: 0
    .symbol:         _Z10state_fastPKtS0_S0_S0_PtS1_Pf.kd
    .uniform_work_group_size: 1
    .uses_dynamic_stack: false
    .vgpr_count:     184
    .vgpr_spill_count: 0
    .wavefront_size: 64
  - .agpr_count:     0
    .args:
      - .actual_access:  read_only
        .address_space:  global
        .offset:         0
        .size:           8
        .value_kind:     global_buffer
      - .actual_access:  read_only
        .address_space:  global
        .offset:         8
        .size:           8
        .value_kind:     global_buffer
      - .actual_access:  read_only
        .address_space:  global
        .offset:         16
        .size:           8
        .value_kind:     global_buffer
      - .actual_access:  write_only
        .address_space:  global
        .offset:         24
        .size:           8
        .value_kind:     global_buffer
      - .actual_access:  write_only
        .address_space:  global
        .offset:         32
        .size:           8
        .value_kind:     global_buffer
      - .actual_access:  write_only
        .address_space:  global
        .offset:         40
        .size:           8
        .value_kind:     global_buffer
    .group_segment_fixed_size: 0
    .kernarg_segment_align: 8
    .kernarg_segment_size: 48
    .language:       OpenCL C
    .language_version:
      - 2
      - 0
    .max_flat_workgroup_size: 256
    .name:           _Z11prefix_fastPKtS0_PKfPtS3_Pf
    .private_segment_fixed_size: 0
    .sgpr_count:     106
    .sgpr_spill_count: 41
    .symbol:         _Z11prefix_fastPKtS0_PKfPtS3_Pf.kd
    .uniform_work_group_size: 1
    .uses_dynamic_stack: false
    .vgpr_count:     205
    .vgpr_spill_count: 0
    .wavefront_size: 64
  - .agpr_count:     0
    .args:
      - .address_space:  global
        .offset:         0
        .size:           8
        .value_kind:     global_buffer
      - .address_space:  global
        .offset:         8
        .size:           8
        .value_kind:     global_buffer
      - .address_space:  global
        .offset:         16
        .size:           8
        .value_kind:     global_buffer
      - .actual_access:  read_only
        .address_space:  global
        .offset:         24
        .size:           8
        .value_kind:     global_buffer
      - .address_space:  global
        .offset:         32
        .size:           8
        .value_kind:     global_buffer
      - .address_space:  global
        .offset:         40
        .size:           8
        .value_kind:     global_buffer
      - .address_space:  global
        .offset:         48
        .size:           8
        .value_kind:     global_buffer
      - .address_space:  global
        .offset:         56
        .size:           8
        .value_kind:     global_buffer
      - .address_space:  global
        .offset:         64
        .size:           8
        .value_kind:     global_buffer
      - .address_space:  global
        .offset:         72
        .size:           8
        .value_kind:     global_buffer
      - .address_space:  global
        .offset:         80
        .size:           8
        .value_kind:     global_buffer
      - .actual_access:  write_only
        .address_space:  global
        .offset:         88
        .size:           8
        .value_kind:     global_buffer
    .group_segment_fixed_size: 0
    .kernarg_segment_align: 8
    .kernarg_segment_size: 96
    .language:       OpenCL C
    .language_version:
      - 2
      - 0
    .max_flat_workgroup_size: 512
    .name:           _Z9attn_fastPKtS0_S0_S0_S0_S0_S0_S0_S0_PKfS2_Pt
    .private_segment_fixed_size: 0
    .sgpr_count:     52
    .sgpr_spill_count: 0
    .symbol:         _Z9attn_fastPKtS0_S0_S0_S0_S0_S0_S0_S0_PKfS2_Pt.kd
    .uniform_work_group_size: 1
    .uses_dynamic_stack: false
    .vgpr_count:     224
    .vgpr_spill_count: 0
    .wavefront_size: 64
  - .agpr_count:     12
    .args:
      - .actual_access:  read_only
        .address_space:  global
        .offset:         0
        .size:           8
        .value_kind:     global_buffer
      - .actual_access:  read_only
        .address_space:  global
        .offset:         8
        .size:           8
        .value_kind:     global_buffer
      - .actual_access:  read_only
        .address_space:  global
        .offset:         16
        .size:           8
        .value_kind:     global_buffer
      - .actual_access:  read_only
        .address_space:  global
        .offset:         24
        .size:           8
        .value_kind:     global_buffer
      - .actual_access:  read_only
        .address_space:  global
        .offset:         32
        .size:           8
        .value_kind:     global_buffer
      - .actual_access:  read_only
        .address_space:  global
        .offset:         40
        .size:           8
        .value_kind:     global_buffer
      - .actual_access:  read_only
        .address_space:  global
        .offset:         48
        .size:           8
        .value_kind:     global_buffer
      - .actual_access:  read_only
        .address_space:  global
        .offset:         56
        .size:           8
        .value_kind:     global_buffer
      - .actual_access:  read_only
        .address_space:  global
        .offset:         64
        .size:           8
        .value_kind:     global_buffer
      - .actual_access:  read_only
        .address_space:  global
        .offset:         72
        .size:           8
        .value_kind:     global_buffer
      - .actual_access:  read_only
        .address_space:  global
        .offset:         80
        .size:           8
        .value_kind:     global_buffer
      - .actual_access:  read_only
        .address_space:  global
        .offset:         88
        .size:           8
        .value_kind:     global_buffer
      - .actual_access:  write_only
        .address_space:  global
        .offset:         96
        .size:           8
        .value_kind:     global_buffer
      - .actual_access:  write_only
        .address_space:  global
        .offset:         104
        .size:           8
        .value_kind:     global_buffer
      - .actual_access:  write_only
        .address_space:  global
        .offset:         112
        .size:           8
        .value_kind:     global_buffer
      - .actual_access:  write_only
        .address_space:  global
        .offset:         120
        .size:           8
        .value_kind:     global_buffer
      - .actual_access:  write_only
        .address_space:  global
        .offset:         128
        .size:           8
        .value_kind:     global_buffer
      - .actual_access:  write_only
        .address_space:  global
        .offset:         136
        .size:           8
        .value_kind:     global_buffer
    .group_segment_fixed_size: 16640
    .kernarg_segment_align: 8
    .kernarg_segment_size: 144
    .language:       OpenCL C
    .language_version:
      - 2
      - 0
    .max_flat_workgroup_size: 256
    .name:           _Z11prep_kernelPKfS0_S0_S0_S0_S0_S0_S0_S0_S0_S0_S0_PtS1_S1_S1_S1_S1_
    .private_segment_fixed_size: 0
    .sgpr_count:     34
    .sgpr_spill_count: 0
    .symbol:         _Z11prep_kernelPKfS0_S0_S0_S0_S0_S0_S0_S0_S0_S0_S0_PtS1_S1_S1_S1_S1_.kd
    .uniform_work_group_size: 1
    .uses_dynamic_stack: false
    .vgpr_count:     124
    .vgpr_spill_count: 0
    .wavefront_size: 64
  - .agpr_count:     0
    .args:
      - .address_space:  global
        .offset:         0
        .size:           8
        .value_kind:     global_buffer
      - .address_space:  global
        .offset:         8
        .size:           8
        .value_kind:     global_buffer
      - .offset:         16
        .size:           4
        .value_kind:     by_value
      - .offset:         20
        .size:           4
        .value_kind:     by_value
      - .offset:         24
        .size:           4
        .value_kind:     by_value
      - .offset:         28
        .size:           4
        .value_kind:     by_value
      - .address_space:  global
        .offset:         32
        .size:           8
        .value_kind:     global_buffer
    .group_segment_fixed_size: 0
    .kernarg_segment_align: 8
    .kernarg_segment_size: 40
    .language:       OpenCL C
    .language_version:
      - 2
      - 0
    .max_flat_workgroup_size: 1024
    .name:           _Z9dbg_cmp16PKtS0_iiffPf
    .private_segment_fixed_size: 0
    .sgpr_count:     18
    .sgpr_spill_count: 0
    .symbol:         _Z9dbg_cmp16PKtS0_iiffPf.kd
    .uniform_work_group_size: 1
    .uses_dynamic_stack: false
    .vgpr_count:     5
    .vgpr_spill_count: 0
    .wavefront_size: 64
  - .agpr_count:     0
    .args:
      - .address_space:  global
        .offset:         0
        .size:           8
        .value_kind:     global_buffer
      - .address_space:  global
        .offset:         8
        .size:           8
        .value_kind:     global_buffer
      - .offset:         16
        .size:           4
        .value_kind:     by_value
      - .offset:         20
        .size:           4
        .value_kind:     by_value
      - .offset:         24
        .size:           56
        .value_kind:     by_value
    .group_segment_fixed_size: 0
    .kernarg_segment_align: 8
    .kernarg_segment_size: 80
    .language:       OpenCL C
    .language_version:
      - 2
      - 0
    .max_flat_workgroup_size: 512
    .name:           _Z5gemm8ILi0EEvPKtS1_ii7EpiArgs
    .private_segment_fixed_size: 0
    .sgpr_count:     36
    .sgpr_spill_count: 0
    .symbol:         _Z5gemm8ILi0EEvPKtS1_ii7EpiArgs.kd
    .uniform_work_group_size: 1
    .uses_dynamic_stack: false
    .vgpr_count:     246
    .vgpr_spill_count: 0
    .wavefront_size: 64
  - .agpr_count:     0
    .args:
      - .address_space:  global
        .offset:         0
        .size:           8
        .value_kind:     global_buffer
      - .address_space:  global
        .offset:         8
        .size:           8
        .value_kind:     global_buffer
      - .address_space:  global
        .offset:         16
        .size:           8
        .value_kind:     global_buffer
      - .address_space:  global
        .offset:         24
        .size:           8
        .value_kind:     global_buffer
      - .actual_access:  write_only
        .address_space:  global
        .offset:         32
        .size:           8
        .value_kind:     global_buffer
      - .actual_access:  write_only
        .address_space:  global
        .offset:         40
        .size:           8
        .value_kind:     global_buffer
      - .actual_access:  write_only
        .address_space:  global
        .offset:         48
        .size:           8
        .value_kind:     global_buffer
    .group_segment_fixed_size: 81920
    .kernarg_segment_align: 8
    .kernarg_segment_size: 56
    .language:       OpenCL C
    .language_version:
      - 2
      - 0
    .max_flat_workgroup_size: 256
    .name:           _Z9scan_fastILb1EEvPKtS1_S1_S1_PtS2_Pf
    .private_segment_fixed_size: 0
    .sgpr_count:     62
    .sgpr_spill_count: 0
    .symbol:         _Z9scan_fastILb1EEvPKtS1_S1_S1_PtS2_Pf.kd
    .uniform_work_group_size: 1
    .uses_dynamic_stack: false
    .vgpr_count:     160
    .vgpr_spill_count: 0
    .wavefront_size: 64
